# speedup vs baseline: 1.0037x; 1.0037x over previous
.LBB1_2:
	s_lshl_b64 s[8:9], s[2:3], 8
	s_lshr_b64 s[6:7], s[8:9], 11
	s_and_b32 s2, s6, 0x1ffffff0
	v_or_b32_e32 v66, s8, v0
	s_lshl_b64 s[10:11], s[2:3], 19
	v_and_b32_e32 v1, 0x7fff, v66
	s_waitcnt lgkmcnt(0)
	v_and_b32_e32 v82, 31, v0
	v_lshlrev_b32_e32 v82, 4, v82
	v_lshrrev_b32_e32 v83, 5, v0
	v_lshl_or_b32 v80, v83, 13, v82
	v_lshl_or_b32 v81, v83, 9, v82
	s_lshl_b32 s14, s2, 12
	s_sub_u32 s12, s12, 0x20000
	s_subb_u32 s13, s13, 0
	s_add_u32 s12, s12, s14
	s_addc_u32 s13, s13, 0
	s_add_u32 s14, s12, 0x1000
	s_addc_u32 s15, s13, 0
	global_load_dwordx4 v[88:91], v80, s[12:13] offset:0
	global_load_dwordx4 v[92:95], v80, s[12:13] offset:512
	global_load_dwordx4 v[96:99], v80, s[12:13] offset:1024
	global_load_dwordx4 v[100:103], v80, s[12:13] offset:1536
	global_load_dwordx4 v[104:107], v80, s[12:13] offset:2048
	global_load_dwordx4 v[108:111], v80, s[12:13] offset:2560
	global_load_dwordx4 v[112:115], v80, s[12:13] offset:3072
	global_load_dwordx4 v[116:119], v80, s[12:13] offset:3584
	global_load_dwordx4 v[120:123], v80, s[14:15] offset:0
	global_load_dwordx4 v[124:127], v80, s[14:15] offset:512
	global_load_dwordx4 v[128:131], v80, s[14:15] offset:1024
	global_load_dwordx4 v[132:135], v80, s[14:15] offset:1536
	global_load_dwordx4 v[136:139], v80, s[14:15] offset:2048
	global_load_dwordx4 v[140:143], v80, s[14:15] offset:2560
	global_load_dwordx4 v[144:147], v80, s[14:15] offset:3072
	global_load_dwordx4 v[148:151], v80, s[14:15] offset:3584
	s_add_u32 s4, s4, s10
	s_addc_u32 s5, s5, s11
	v_lshlrev_b32_e32 v68, 4, v1
	v_lshl_add_u64 v[14:15], s[4:5], 0, v[68:69]
	s_mov_b32 s8, 0x80000
	v_add_co_u32_e32 v2, vcc, s8, v14
	s_mov_b32 s8, 0x100000
	s_nop 0
	v_addc_co_u32_e32 v3, vcc, 0, v15, vcc
	v_add_co_u32_e32 v4, vcc, s8, v14
	s_mov_b32 s8, 0x180000
	s_nop 0
	v_addc_co_u32_e32 v5, vcc, 0, v15, vcc
	global_load_dwordx4 v[42:45], v[2:3], off nt
	global_load_dwordx4 v[34:37], v[4:5], off nt
	v_add_co_u32_e32 v2, vcc, s8, v14
	s_mov_b32 s8, 0x200000
	s_nop 0
	v_addc_co_u32_e32 v3, vcc, 0, v15, vcc
	v_add_co_u32_e32 v4, vcc, s8, v14
	s_mov_b32 s8, 0x280000
	s_nop 0
	v_addc_co_u32_e32 v5, vcc, 0, v15, vcc
	global_load_dwordx4 v[58:61], v[2:3], off nt
	global_load_dwordx4 v[46:49], v[4:5], off nt
	v_add_co_u32_e32 v2, vcc, s8, v14
	s_mov_b32 s8, 0x300000
	s_nop 0
	v_addc_co_u32_e32 v3, vcc, 0, v15, vcc
	v_add_co_u32_e32 v4, vcc, s8, v14
	s_mov_b32 s8, 0x380000
	s_nop 0
	v_addc_co_u32_e32 v5, vcc, 0, v15, vcc
	v_add_co_u32_e32 v6, vcc, s8, v14
	s_mov_b32 s8, 0x400000
	s_nop 0
	v_addc_co_u32_e32 v7, vcc, 0, v15, vcc
	v_add_co_u32_e32 v8, vcc, s8, v14
	s_mov_b32 s8, 0x480000
	s_nop 0
	v_addc_co_u32_e32 v9, vcc, 0, v15, vcc
	v_add_co_u32_e32 v16, vcc, s8, v14
	s_mov_b32 s8, 0x500000
	s_nop 0
	v_addc_co_u32_e32 v17, vcc, 0, v15, vcc
	v_add_co_u32_e32 v18, vcc, s8, v14
	s_mov_b32 s8, 0x580000
	s_nop 0
	v_addc_co_u32_e32 v19, vcc, 0, v15, vcc
	v_add_co_u32_e32 v70, vcc, s8, v14
	s_mov_b32 s8, 0x600000
	s_nop 0
	v_addc_co_u32_e32 v71, vcc, 0, v15, vcc
	v_add_co_u32_e32 v72, vcc, s8, v14
	s_mov_b32 s8, 0x680000
	s_nop 0
	v_addc_co_u32_e32 v73, vcc, 0, v15, vcc
	v_add_co_u32_e32 v74, vcc, s8, v14
	global_load_dwordx4 v[54:57], v[2:3], off nt
	global_load_dwordx4 v[38:41], v[4:5], off nt
	v_addc_co_u32_e32 v75, vcc, 0, v15, vcc
	v_add_co_u32_e32 v76, vcc, 0x700000, v14
	global_load_dwordx4 v[50:53], v[6:7], off nt
	global_load_dwordx4 v[2:5], v[8:9], off nt
	v_addc_co_u32_e32 v77, vcc, 0, v15, vcc
	v_add_co_u32_e32 v78, vcc, 0x780000, v14
	global_load_dwordx4 v[10:13], v[16:17], off nt
	global_load_dwordx4 v[6:9], v[18:19], off nt
	v_addc_co_u32_e32 v79, vcc, 0, v15, vcc
	global_load_dwordx4 v[30:33], v[70:71], off nt
	global_load_dwordx4 v[22:25], v[72:73], off nt
	global_load_dwordx4 v[26:29], v[74:75], off nt
	global_load_dwordx4 v[18:21], v[76:77], off nt
	global_load_dwordx4 v[62:65], v68, s[4:5] nt
	global_load_dwordx4 v[14:17], v[78:79], off nt
	s_load_dwordx2 s[4:5], s[0:1], 0x18
	v_mov_b32_e32 v67, s9
	s_waitcnt lgkmcnt(0)
	s_waitcnt vmcnt(31)
	s_waitcnt vmcnt(30)
	v_pk_add_f32 v[88:89], v[88:89], v[92:93]
	v_pk_add_f32 v[90:91], v[90:91], v[94:95]
	s_waitcnt vmcnt(29)
	v_pk_add_f32 v[88:89], v[88:89], v[96:97]
	v_pk_add_f32 v[90:91], v[90:91], v[98:99]
	s_waitcnt vmcnt(28)
	v_pk_add_f32 v[88:89], v[88:89], v[100:101]
	v_pk_add_f32 v[90:91], v[90:91], v[102:103]
	s_waitcnt vmcnt(27)
	v_pk_add_f32 v[88:89], v[88:89], v[104:105]
	v_pk_add_f32 v[90:91], v[90:91], v[106:107]
	s_waitcnt vmcnt(26)
	v_pk_add_f32 v[88:89], v[88:89], v[108:109]
	v_pk_add_f32 v[90:91], v[90:91], v[110:111]
	s_waitcnt vmcnt(25)
	v_pk_add_f32 v[88:89], v[88:89], v[112:113]
	v_pk_add_f32 v[90:91], v[90:91], v[114:115]
	s_waitcnt vmcnt(24)
	v_pk_add_f32 v[88:89], v[88:89], v[116:117]
	v_pk_add_f32 v[90:91], v[90:91], v[118:119]
	s_waitcnt vmcnt(23)
	v_pk_add_f32 v[88:89], v[88:89], v[120:121]
	v_pk_add_f32 v[90:91], v[90:91], v[122:123]
	s_waitcnt vmcnt(22)
	v_pk_add_f32 v[88:89], v[88:89], v[124:125]
	v_pk_add_f32 v[90:91], v[90:91], v[126:127]
	s_waitcnt vmcnt(21)
	v_pk_add_f32 v[88:89], v[88:89], v[128:129]
	v_pk_add_f32 v[90:91], v[90:91], v[130:131]
	s_waitcnt vmcnt(20)
	v_pk_add_f32 v[88:89], v[88:89], v[132:133]
	v_pk_add_f32 v[90:91], v[90:91], v[134:135]
	s_waitcnt vmcnt(19)
	v_pk_add_f32 v[88:89], v[88:89], v[136:137]
	v_pk_add_f32 v[90:91], v[90:91], v[138:139]
	s_waitcnt vmcnt(18)
	v_pk_add_f32 v[88:89], v[88:89], v[140:141]
	v_pk_add_f32 v[90:91], v[90:91], v[142:143]
	s_waitcnt vmcnt(17)
	v_pk_add_f32 v[88:89], v[88:89], v[144:145]
	v_pk_add_f32 v[90:91], v[90:91], v[146:147]
	s_waitcnt vmcnt(16)
	v_pk_add_f32 v[88:89], v[88:89], v[148:149]
	v_pk_add_f32 v[90:91], v[90:91], v[150:151]
	ds_write_b128 v81, v[88:91] offset:512
	s_waitcnt lgkmcnt(0)
	s_barrier
	s_movk_i32 s8, 0x80
	v_cmp_gt_u32_e32 vcc, s8, v0
	s_and_saveexec_b64 s[8:9], vcc
	s_cbranch_execz .LBB1_4
	v_lshlrev_b32_e32 v68, 2, v0
	ds_read_b32 v74, v68 offset:512
	ds_read_b32 v75, v68 offset:1024
	ds_read_b32 v76, v68 offset:1536
	ds_read_b32 v77, v68 offset:2048
	ds_read_b32 v78, v68 offset:2560
	ds_read_b32 v79, v68 offset:3072
	ds_read_b32 v80, v68 offset:3584
	ds_read_b32 v81, v68 offset:4096
	s_waitcnt lgkmcnt(0)
	v_add_f32_e32 v1, 0, v74
	v_add_f32_e32 v1, v1, v75
	v_add_f32_e32 v1, v1, v76
	v_add_f32_e32 v1, v1, v77
	v_add_f32_e32 v1, v1, v78
	v_add_f32_e32 v1, v1, v79
	v_add_f32_e32 v1, v1, v80
	v_add_f32_e32 v1, v1, v81
	v_mul_f32_e32 v1, 0x3bf00000, v1
	ds_write_b32 v68, v1
.LBB1_4:
	s_or_b64 exec, exec, s[8:9]
	v_lshlrev_b32_e32 v0, 5, v0
	v_and_b32_e32 v0, 0x1e0, v0
	s_waitcnt lgkmcnt(0)
	s_barrier
	ds_read_b128 v[68:71], v0
	ds_read_b128 v[72:75], v0 offset:16
	s_waitcnt vmcnt(1)
	v_lshlrev_b32_e32 v0, 16, v62
	v_and_b32_e32 v1, 0xffff0000, v62
	v_lshlrev_b32_e32 v62, 16, v63
	v_and_b32_e32 v63, 0xffff0000, v63
	s_waitcnt lgkmcnt(1)
	v_pk_add_f32 v[0:1], v[68:69], v[0:1]
	v_lshlrev_b32_e32 v68, 16, v42
	v_and_b32_e32 v69, 0xffff0000, v42
	v_pk_add_f32 v[62:63], v[70:71], v[62:63]
	v_lshlrev_b32_e32 v42, 16, v43
	v_and_b32_e32 v43, 0xffff0000, v43
	v_pk_add_f32 v[0:1], v[0:1], v[68:69]
	v_lshlrev_b32_e32 v68, 16, v34
	v_and_b32_e32 v69, 0xffff0000, v34
	v_pk_add_f32 v[42:43], v[62:63], v[42:43]
	v_lshlrev_b32_e32 v34, 16, v35
	v_and_b32_e32 v35, 0xffff0000, v35
	v_pk_add_f32 v[34:35], v[42:43], v[34:35]
	v_lshlrev_b32_e32 v42, 16, v59
	v_and_b32_e32 v43, 0xffff0000, v59
	v_pk_add_f32 v[34:35], v[34:35], v[42:43]
	v_lshlrev_b32_e32 v42, 16, v47
	v_and_b32_e32 v43, 0xffff0000, v47
	v_pk_add_f32 v[0:1], v[0:1], v[68:69]
	v_lshlrev_b32_e32 v68, 16, v58
	v_and_b32_e32 v69, 0xffff0000, v58
	v_pk_add_f32 v[34:35], v[34:35], v[42:43]
	v_lshlrev_b32_e32 v42, 16, v64
	v_and_b32_e32 v43, 0xffff0000, v64
	v_pk_add_f32 v[0:1], v[0:1], v[68:69]
	v_lshlrev_b32_e32 v68, 16, v46
	v_and_b32_e32 v69, 0xffff0000, v46
	s_waitcnt lgkmcnt(0)
	v_pk_add_f32 v[42:43], v[72:73], v[42:43]
	v_lshlrev_b32_e32 v46, 16, v44
	v_and_b32_e32 v47, 0xffff0000, v44
	v_pk_add_f32 v[42:43], v[42:43], v[46:47]
	v_lshlrev_b32_e32 v46, 16, v36
	v_and_b32_e32 v47, 0xffff0000, v36
	v_pk_add_f32 v[42:43], v[42:43], v[46:47]
	v_lshlrev_b32_e32 v46, 16, v60
	v_and_b32_e32 v47, 0xffff0000, v60
	v_pk_add_f32 v[42:43], v[42:43], v[46:47]
	v_lshlrev_b32_e32 v46, 16, v48
	v_and_b32_e32 v47, 0xffff0000, v48
	v_pk_add_f32 v[42:43], v[42:43], v[46:47]
	v_lshlrev_b32_e32 v46, 16, v65
	v_and_b32_e32 v47, 0xffff0000, v65
	v_pk_add_f32 v[46:47], v[74:75], v[46:47]
	v_lshlrev_b32_e32 v44, 16, v45
	v_and_b32_e32 v45, 0xffff0000, v45
	v_pk_add_f32 v[44:45], v[46:47], v[44:45]
	v_lshlrev_b32_e32 v36, 16, v37
	v_and_b32_e32 v37, 0xffff0000, v37
	v_pk_add_f32 v[36:37], v[44:45], v[36:37]
	v_lshlrev_b32_e32 v44, 16, v61
	v_and_b32_e32 v45, 0xffff0000, v61
	v_pk_add_f32 v[36:37], v[36:37], v[44:45]
	v_lshlrev_b32_e32 v44, 16, v49
	v_and_b32_e32 v45, 0xffff0000, v49
	v_pk_add_f32 v[0:1], v[0:1], v[68:69]
	v_pk_add_f32 v[36:37], v[36:37], v[44:45]
	v_lshlrev_b32_e32 v44, 16, v54
	v_and_b32_e32 v45, 0xffff0000, v54
	v_lshlrev_b32_e32 v46, 16, v55
	v_and_b32_e32 v47, 0xffff0000, v55
	v_lshlrev_b32_e32 v48, 16, v56
	v_and_b32_e32 v49, 0xffff0000, v56
	v_lshlrev_b32_e32 v54, 16, v57
	v_and_b32_e32 v55, 0xffff0000, v57
	v_lshlrev_b32_e32 v56, 16, v38
	v_and_b32_e32 v57, 0xffff0000, v38
	v_lshlrev_b32_e32 v38, 16, v39
	v_and_b32_e32 v39, 0xffff0000, v39
	v_pk_add_f32 v[0:1], v[0:1], v[44:45]
	v_pk_add_f32 v[34:35], v[34:35], v[46:47]
	v_lshlrev_b32_e32 v60, 16, v50
	v_and_b32_e32 v61, 0xffff0000, v50
	v_lshlrev_b32_e32 v50, 16, v51
	v_and_b32_e32 v51, 0xffff0000, v51
	v_pk_add_f32 v[0:1], v[0:1], v[56:57]
	v_pk_add_f32 v[34:35], v[34:35], v[38:39]
	v_pk_add_f32 v[0:1], v[0:1], v[60:61]
	v_lshlrev_b32_e32 v44, 16, v2
	v_and_b32_e32 v45, 0xffff0000, v2
	v_pk_add_f32 v[34:35], v[34:35], v[50:51]
	v_lshlrev_b32_e32 v2, 16, v3
	v_and_b32_e32 v3, 0xffff0000, v3
	v_pk_add_f32 v[0:1], v[0:1], v[44:45]
	v_lshlrev_b32_e32 v44, 16, v10
	v_and_b32_e32 v45, 0xffff0000, v10
	v_pk_add_f32 v[2:3], v[34:35], v[2:3]
	v_lshlrev_b32_e32 v10, 16, v11
	v_and_b32_e32 v11, 0xffff0000, v11
	v_pk_add_f32 v[0:1], v[0:1], v[44:45]
	v_lshlrev_b32_e32 v44, 16, v6
	v_and_b32_e32 v45, 0xffff0000, v6
	v_pk_add_f32 v[2:3], v[2:3], v[10:11]
	v_lshlrev_b32_e32 v6, 16, v7
	v_and_b32_e32 v7, 0xffff0000, v7
	v_pk_add_f32 v[2:3], v[2:3], v[6:7]
	v_lshlrev_b32_e32 v6, 16, v31
	v_and_b32_e32 v7, 0xffff0000, v31
	v_pk_add_f32 v[2:3], v[2:3], v[6:7]
	v_lshlrev_b32_e32 v6, 16, v23
	v_and_b32_e32 v7, 0xffff0000, v23
	v_pk_add_f32 v[2:3], v[2:3], v[6:7]
	v_lshlrev_b32_e32 v6, 16, v27
	v_and_b32_e32 v7, 0xffff0000, v27
	v_pk_add_f32 v[2:3], v[2:3], v[6:7]
	v_lshlrev_b32_e32 v6, 16, v19
	v_and_b32_e32 v7, 0xffff0000, v19
	v_pk_add_f32 v[2:3], v[2:3], v[6:7]
	s_waitcnt vmcnt(0)
	v_lshlrev_b32_e32 v6, 16, v15
	v_and_b32_e32 v7, 0xffff0000, v15
	v_lshlrev_b32_e32 v58, 16, v40
	v_and_b32_e32 v59, 0xffff0000, v40
	v_pk_add_f32 v[2:3], v[2:3], v[6:7]
	v_pk_add_f32 v[6:7], v[42:43], v[48:49]
	v_lshlrev_b32_e32 v62, 16, v52
	v_and_b32_e32 v63, 0xffff0000, v52
	v_pk_add_f32 v[6:7], v[6:7], v[58:59]
	v_lshlrev_b32_e32 v10, 16, v4
	v_pk_add_f32 v[6:7], v[6:7], v[62:63]
	v_and_b32_e32 v11, 0xffff0000, v4
	v_pk_add_f32 v[6:7], v[6:7], v[10:11]
	v_lshlrev_b32_e32 v10, 16, v12
	v_and_b32_e32 v11, 0xffff0000, v12
	v_pk_add_f32 v[6:7], v[6:7], v[10:11]
	v_lshlrev_b32_e32 v10, 16, v8
	v_and_b32_e32 v11, 0xffff0000, v8
	v_pk_add_f32 v[6:7], v[6:7], v[10:11]
	v_lshlrev_b32_e32 v10, 16, v32
	v_and_b32_e32 v11, 0xffff0000, v32
	v_pk_add_f32 v[6:7], v[6:7], v[10:11]
	v_lshlrev_b32_e32 v10, 16, v24
	v_and_b32_e32 v11, 0xffff0000, v24
	v_pk_add_f32 v[6:7], v[6:7], v[10:11]
	v_lshlrev_b32_e32 v10, 16, v28
	v_and_b32_e32 v11, 0xffff0000, v28
	v_pk_add_f32 v[6:7], v[6:7], v[10:11]
	v_lshlrev_b32_e32 v10, 16, v20
	v_and_b32_e32 v11, 0xffff0000, v20
	v_pk_add_f32 v[6:7], v[6:7], v[10:11]
	v_lshlrev_b32_e32 v10, 16, v16
	v_and_b32_e32 v11, 0xffff0000, v16
	v_lshlrev_b32_e32 v40, 16, v41
	v_and_b32_e32 v41, 0xffff0000, v41
	v_pk_add_f32 v[6:7], v[6:7], v[10:11]
	v_pk_add_f32 v[10:11], v[36:37], v[54:55]
	v_lshlrev_b32_e32 v52, 16, v53
	v_and_b32_e32 v53, 0xffff0000, v53
	v_pk_add_f32 v[10:11], v[10:11], v[40:41]
	v_lshlrev_b32_e32 v4, 16, v5
	v_pk_add_f32 v[10:11], v[10:11], v[52:53]
	v_and_b32_e32 v5, 0xffff0000, v5
	v_pk_add_f32 v[4:5], v[10:11], v[4:5]
	v_lshlrev_b32_e32 v10, 16, v13
	v_and_b32_e32 v11, 0xffff0000, v13
	v_pk_add_f32 v[4:5], v[4:5], v[10:11]
	v_lshlrev_b32_e32 v8, 16, v9
	v_and_b32_e32 v9, 0xffff0000, v9
	v_pk_add_f32 v[4:5], v[4:5], v[8:9]
	v_lshlrev_b32_e32 v8, 16, v33
	v_and_b32_e32 v9, 0xffff0000, v33
	v_pk_add_f32 v[0:1], v[0:1], v[44:45]
	v_lshlrev_b32_e32 v44, 16, v30
	v_and_b32_e32 v45, 0xffff0000, v30
	v_pk_add_f32 v[4:5], v[4:5], v[8:9]
	v_lshlrev_b32_e32 v8, 16, v25
	v_and_b32_e32 v9, 0xffff0000, v25
	v_pk_add_f32 v[0:1], v[0:1], v[44:45]
	v_lshlrev_b32_e32 v44, 16, v22
	v_and_b32_e32 v45, 0xffff0000, v22
	v_pk_add_f32 v[4:5], v[4:5], v[8:9]
	v_lshlrev_b32_e32 v8, 16, v29
	v_and_b32_e32 v9, 0xffff0000, v29
	v_pk_add_f32 v[0:1], v[0:1], v[44:45]
	v_lshlrev_b32_e32 v44, 16, v26
	v_and_b32_e32 v45, 0xffff0000, v26
	v_pk_add_f32 v[4:5], v[4:5], v[8:9]
	v_lshlrev_b32_e32 v8, 16, v21
	v_and_b32_e32 v9, 0xffff0000, v21
	v_pk_add_f32 v[0:1], v[0:1], v[44:45]
	v_lshlrev_b32_e32 v44, 16, v18
	v_and_b32_e32 v45, 0xffff0000, v18
	v_pk_add_f32 v[4:5], v[4:5], v[8:9]
	v_lshlrev_b32_e32 v8, 16, v17
	v_and_b32_e32 v9, 0xffff0000, v17
	v_pk_add_f32 v[0:1], v[0:1], v[44:45]
	v_lshlrev_b32_e32 v44, 16, v14
	v_and_b32_e32 v45, 0xffff0000, v14
	v_pk_add_f32 v[8:9], v[4:5], v[8:9]
	v_lshlrev_b64 v[4:5], 5, v[66:67]
	v_pk_add_f32 v[0:1], v[0:1], v[44:45]
	v_lshl_add_u64 v[4:5], s[4:5], 0, v[4:5]
	global_store_dwordx4 v[4:5], v[0:3], off nt
	global_store_dwordx4 v[4:5], v[6:9], off offset:16 nt
	s_endpgm
